# gcn2 loop: bias SrcC tuples via per-wave LDS table (ds_read_b128 per column tile) instead of 4 v_mov; ct pipeline regenerated
# speedup vs baseline: 1.0106x; 1.0020x over previous
.LBB5_16:
	v_cmp_ne_u32_e32 vcc, 0, v1
	v_lshlrev_b32_e32 v87, 4, v79
	v_add_u32_e32 v66, 0x5900, v3
	v_and_b32_e32 v85, 63, v78
	v_and_b32_e32 v86, 15, v78
	v_bfe_u32 v83, v78, 4, 2
	s_cbranch_vccz .LBB5_42
	v_sub_u32_e32 v0, v65, v64
	v_or_b32_e32 v88, v87, v86
	v_add_u32_e32 v91, v0, v2
	v_lshlrev_b32_e32 v90, 2, v88
	ds_read_b32 v84, v90 offset:22528
	v_add_u32_e32 v0, 15, v91
	v_ashrrev_i32_e32 v92, 4, v0
	v_add_u32_e32 v0, 2, v92
	v_ashrrev_i32_e32 v93, 1, v0
	v_cmp_gt_i32_e32 vcc, 1, v93
	v_lshlrev_b32_e32 v89, 2, v83
	s_and_saveexec_b64 s[4:5], vcc
	s_xor_b64 s[4:5], exec, s[4:5]
	v_lshlrev_b32_e32 v89, 2, v83
	s_or_saveexec_b64 s[6:7], s[4:5]
	v_mov_b32_e32 v3, 0
	v_mov_b32_e32 v2, v3
	v_mov_b32_e32 v1, v3
	v_mov_b32_e32 v0, v3
	v_mov_b32_e32 v7, v3
	v_mov_b32_e32 v6, v3
	v_mov_b32_e32 v5, v3
	v_mov_b32_e32 v4, v3
	v_mov_b32_e32 v11, v3
	v_mov_b32_e32 v10, v3
	v_mov_b32_e32 v9, v3
	v_mov_b32_e32 v8, v3
	v_mov_b32_e32 v15, v3
	v_mov_b32_e32 v14, v3
	v_mov_b32_e32 v13, v3
	v_mov_b32_e32 v12, v3
	v_mov_b32_e32 v19, v3
	v_mov_b32_e32 v18, v3
	v_mov_b32_e32 v17, v3
	v_mov_b32_e32 v16, v3
	v_mov_b32_e32 v23, v3
	v_mov_b32_e32 v22, v3
	v_mov_b32_e32 v21, v3
	v_mov_b32_e32 v20, v3
	v_mov_b32_e32 v27, v3
	v_mov_b32_e32 v26, v3
	v_mov_b32_e32 v25, v3
	v_mov_b32_e32 v24, v3
	v_mov_b32_e32 v31, v3
	v_mov_b32_e32 v30, v3
	v_mov_b32_e32 v29, v3
	v_mov_b32_e32 v28, v3
	s_xor_b64 exec, exec, s[6:7]
	s_cbranch_execz .LBB5_44
	v_lshlrev_b32_e32 v0, 4, v85
	v_mov_b32_e32 v1, 0
	v_lshl_add_u64 v[2:3], s[12:13], 0, v[0:1]
	s_movk_i32 s4, 0x1000
	v_lshlrev_b32_e32 v4, 2, v86
	v_add_co_u32_e32 v2, vcc, s4, v2
	global_load_dwordx4 v[32:35], v0, s[12:13]
	global_load_dwordx4 v[36:39], v0, s[12:13] offset:1024
	global_load_dwordx4 v[40:43], v0, s[12:13] offset:2048
	global_load_dwordx4 v[44:47], v0, s[12:13] offset:3072
	v_addc_co_u32_e32 v3, vcc, 0, v3, vcc
	global_load_dword v65, v4, s[14:15]
	global_load_dword v94, v4, s[14:15] offset:64
	global_load_dword v95, v4, s[14:15] offset:128
	global_load_dword v96, v4, s[14:15] offset:192
	global_load_dword v97, v4, s[14:15] offset:256
	global_load_dword v98, v4, s[14:15] offset:320
	global_load_dword v99, v4, s[14:15] offset:384
	global_load_dword v100, v4, s[14:15] offset:448
	global_load_dwordx4 v[48:51], v[2:3], off
	global_load_dwordx4 v[52:55], v[2:3], off offset:1024
	global_load_dwordx4 v[56:59], v[2:3], off offset:2048
	global_load_dwordx4 v[60:63], v[2:3], off offset:3072
	ds_read2st64_b32 v[2:3], v90 offset0:89 offset1:90
	ds_read_b32 v0, v66
	v_cmp_eq_u32_e32 vcc, v89, v86
	v_lshlrev_b32_e32 v4, 3, v82
	s_mov_b32 s4, 0x5040100
	s_mov_b32 s28, 0
	s_waitcnt lgkmcnt(0)
	v_sub_u32_e32 v101, v2, v0
	v_cvt_f16_f32_e32 v2, v84
	v_add_u32_e32 v102, v101, v3
	v_add_u32_e32 v3, s3, v87
	v_sub_u32_e32 v0, v64, v82
	v_or_b32_e32 v103, v3, v86
	v_mov_b32_e32 v3, 0x4400
	v_lshl_add_u32 v104, v0, 3, v3
	v_or_b32_e32 v0, 2, v89
	v_cndmask_b32_e32 v66, 0, v2, vcc
	v_or_b32_e32 v3, 1, v89
	v_cmp_eq_u32_e32 vcc, v0, v86
	s_mov_b64 s[12:13], 0
	s_mov_b32 s29, 0
	v_cndmask_b32_e32 v0, 0, v2, vcc
	v_cmp_eq_u32_e32 vcc, v3, v86
	v_or_b32_e32 v3, 3, v89
	v_mov_b32_e32 v28, v1
	v_cndmask_b32_e32 v67, 0, v2, vcc
	v_cmp_eq_u32_e32 vcc, v3, v86
	v_lshlrev_b32_e32 v3, 3, v86
	v_lshl_add_u32 v3, v64, 3, v3
	v_cndmask_b32_e32 v2, 0, v2, vcc
	v_pack_b32_f16 v105, v0, v2
	v_pack_b32_f16 v0, v67, v0
	v_sub_u32_e32 v3, v3, v4
	v_add_u32_e32 v106, 0x4400, v3
	v_alignbit_b32 v107, v2, v0, 16
	v_perm_b32 v108, v0, v66, s4
	v_mov_b32_e32 v0, v1
	v_mov_b32_e32 v2, v1
	v_mov_b32_e32 v3, v1
	v_mov_b32_e32 v4, v1
	v_and_b32_e32 v109, 48, v78
	v_add_u32_e32 v110, -1, v91
	v_add_u32_e32 v111, -1, v92
	v_pack_b32_f16 v64, v66, v67
	v_readfirstlane_b32 s40, v92
	v_sub_u32_e32 v102, v102, v101
	s_waitcnt vmcnt(4)
	v_lshl_add_u32 v124, v87, 3, v86
	v_lshlrev_b32_e32 v124, 4, v124
	v_add_u32_e32 v124, 0x5d00, v124
	ds_write2_b32 v124, v65, v65 offset0:0 offset1:1
	ds_write2_b32 v124, v65, v65 offset0:2 offset1:3
	ds_write2_b32 v124, v94, v94 offset0:64 offset1:65
	ds_write2_b32 v124, v94, v94 offset0:66 offset1:67
	ds_write2_b32 v124, v95, v95 offset0:128 offset1:129
	ds_write2_b32 v124, v95, v95 offset0:130 offset1:131
	ds_write2_b32 v124, v96, v96 offset0:192 offset1:193
	ds_write2_b32 v124, v96, v96 offset0:194 offset1:195
	v_add_u32_e32 v125, 0x400, v124
	ds_write2_b32 v125, v97, v97 offset0:0 offset1:1
	ds_write2_b32 v125, v97, v97 offset0:2 offset1:3
	ds_write2_b32 v125, v98, v98 offset0:64 offset1:65
	ds_write2_b32 v125, v98, v98 offset0:66 offset1:67
	ds_write2_b32 v125, v99, v99 offset0:128 offset1:129
	ds_write2_b32 v125, v99, v99 offset0:130 offset1:131
	ds_write2_b32 v125, v100, v100 offset0:192 offset1:193
	ds_write2_b32 v125, v100, v100 offset0:194 offset1:195
	v_mov_b32_e32 v98, v124
	s_waitcnt lgkmcnt(0)
	s_nop 3
	s_branch .LBB5_23
.LBB5_22:
	ds_read_b128 v[124:127], v98
	ds_read_b128 v[94:97], v98 offset:256
	global_load_dwordx4 v[74:77], v74, s[10:11]
	s_waitcnt vmcnt(1) lgkmcnt(1)
	v_mfma_f32_16x16x32_f16 v[112:115], v[70:73], v[32:35], v[124:127]
	s_waitcnt vmcnt(0)
	v_mfma_f32_16x16x32_f16 v[116:119], v[74:77], v[32:35], v[124:127]
	ds_read_b128 v[124:127], v98 offset:512
	v_add_u32_e32 v93, -1, v93
	s_add_i32 s29, s29, 32
	s_add_i32 s28, s28, 2
	v_cmp_eq_u32_e32 vcc, 0, v93
	v_add_u32_e32 v106, 0x100, v106
	s_or_b64 s[12:13], vcc, s[12:13]
	v_cvt_pk_f16_f32 v112, v112, v113
	v_cvt_pk_f16_f32 v113, v114, v115
	v_cvt_pk_f16_f32 v114, v116, v117
	v_cvt_pk_f16_f32 v115, v118, v119
	s_waitcnt lgkmcnt(1)
	v_mfma_f32_16x16x32_f16 v[120:123], v[70:73], v[36:39], v[94:97]
	v_mfma_f32_16x16x32_f16 v[116:119], v[74:77], v[36:39], v[94:97]
	v_pk_max_f16 v112, v112, 0
	v_pk_max_f16 v113, v113, 0
	v_pk_max_f16 v114, v114, 0
	v_pk_max_f16 v115, v115, 0
	ds_read_b128 v[94:97], v98 offset:768
	s_waitcnt lgkmcnt(1)
	v_mfma_f32_16x16x32_f16 v[28:31], v[112:115], v[66:69], v[28:31]
	v_cvt_pk_f16_f32 v120, v120, v121
	v_cvt_pk_f16_f32 v121, v122, v123
	v_cvt_pk_f16_f32 v122, v116, v117
	v_cvt_pk_f16_f32 v123, v118, v119
	v_mfma_f32_16x16x32_f16 v[112:115], v[70:73], v[40:43], v[124:127]
	v_mfma_f32_16x16x32_f16 v[116:119], v[74:77], v[40:43], v[124:127]
	v_pk_max_f16 v120, v120, 0
	v_pk_max_f16 v121, v121, 0
	v_pk_max_f16 v122, v122, 0
	v_pk_max_f16 v123, v123, 0
	ds_read_b128 v[124:127], v98 offset:1024
	s_waitcnt lgkmcnt(1)
	v_mfma_f32_16x16x32_f16 v[24:27], v[120:123], v[66:69], v[24:27]
	v_cvt_pk_f16_f32 v112, v112, v113
	v_cvt_pk_f16_f32 v113, v114, v115
	v_cvt_pk_f16_f32 v114, v116, v117
	v_cvt_pk_f16_f32 v115, v118, v119
	v_mfma_f32_16x16x32_f16 v[120:123], v[70:73], v[44:47], v[94:97]
	v_mfma_f32_16x16x32_f16 v[116:119], v[74:77], v[44:47], v[94:97]
	v_pk_max_f16 v112, v112, 0
	v_pk_max_f16 v113, v113, 0
	v_pk_max_f16 v114, v114, 0
	v_pk_max_f16 v115, v115, 0
	ds_read_b128 v[94:97], v98 offset:1280
	s_waitcnt lgkmcnt(1)
	v_mfma_f32_16x16x32_f16 v[20:23], v[112:115], v[66:69], v[20:23]
	v_cvt_pk_f16_f32 v120, v120, v121
	v_cvt_pk_f16_f32 v121, v122, v123
	v_cvt_pk_f16_f32 v122, v116, v117
	v_cvt_pk_f16_f32 v123, v118, v119
	v_mfma_f32_16x16x32_f16 v[112:115], v[70:73], v[48:51], v[124:127]
	v_mfma_f32_16x16x32_f16 v[116:119], v[74:77], v[48:51], v[124:127]
	v_pk_max_f16 v120, v120, 0
	v_pk_max_f16 v121, v121, 0
	v_pk_max_f16 v122, v122, 0
	v_pk_max_f16 v123, v123, 0
	ds_read_b128 v[124:127], v98 offset:1536
	s_waitcnt lgkmcnt(1)
	v_mfma_f32_16x16x32_f16 v[16:19], v[120:123], v[66:69], v[16:19]
	v_cvt_pk_f16_f32 v112, v112, v113
	v_cvt_pk_f16_f32 v113, v114, v115
	v_cvt_pk_f16_f32 v114, v116, v117
	v_cvt_pk_f16_f32 v115, v118, v119
	v_mfma_f32_16x16x32_f16 v[120:123], v[70:73], v[52:55], v[94:97]
	v_mfma_f32_16x16x32_f16 v[116:119], v[74:77], v[52:55], v[94:97]
	v_pk_max_f16 v112, v112, 0
	v_pk_max_f16 v113, v113, 0
	v_pk_max_f16 v114, v114, 0
	v_pk_max_f16 v115, v115, 0
	ds_read_b128 v[94:97], v98 offset:1792
	s_waitcnt lgkmcnt(1)
	v_mfma_f32_16x16x32_f16 v[12:15], v[112:115], v[66:69], v[12:15]
	v_cvt_pk_f16_f32 v120, v120, v121
	v_cvt_pk_f16_f32 v121, v122, v123
	v_cvt_pk_f16_f32 v122, v116, v117
	v_cvt_pk_f16_f32 v123, v118, v119
	v_mfma_f32_16x16x32_f16 v[112:115], v[70:73], v[56:59], v[124:127]
	v_mfma_f32_16x16x32_f16 v[116:119], v[74:77], v[56:59], v[124:127]
	v_pk_max_f16 v120, v120, 0
	v_pk_max_f16 v121, v121, 0
	v_pk_max_f16 v122, v122, 0
	v_pk_max_f16 v123, v123, 0
	s_waitcnt lgkmcnt(0)
	s_nop 0
	v_mfma_f32_16x16x32_f16 v[8:11], v[120:123], v[66:69], v[8:11]
	v_cvt_pk_f16_f32 v112, v112, v113
	v_cvt_pk_f16_f32 v113, v114, v115
	v_cvt_pk_f16_f32 v114, v116, v117
	v_cvt_pk_f16_f32 v115, v118, v119
	v_mfma_f32_16x16x32_f16 v[120:123], v[70:73], v[60:63], v[94:97]
	v_mfma_f32_16x16x32_f16 v[116:119], v[74:77], v[60:63], v[94:97]
	v_pk_max_f16 v112, v112, 0
	v_pk_max_f16 v113, v113, 0
	v_pk_max_f16 v114, v114, 0
	v_pk_max_f16 v115, v115, 0
	s_nop 1
	v_mfma_f32_16x16x32_f16 v[4:7], v[112:115], v[66:69], v[4:7]
	v_cvt_pk_f16_f32 v120, v120, v121
	v_cvt_pk_f16_f32 v121, v122, v123
	v_cvt_pk_f16_f32 v122, v116, v117
	v_cvt_pk_f16_f32 v123, v118, v119
	v_pk_max_f16 v120, v120, 0
	v_pk_max_f16 v121, v121, 0
	v_pk_max_f16 v122, v122, 0
	v_pk_max_f16 v123, v123, 0
	s_nop 1
	v_mfma_f32_16x16x32_f16 v[0:3], v[120:123], v[66:69], v[0:3]
	s_andn2_b64 exec, exec, s[12:13]
	s_cbranch_execz .LBB5_43

	.amdhsa_kernel _Z5k_gcnILi2EEvPKvPK15HIP_vector_typeIiLj2EEPfPKiS8_PKfPKDF16_SA_SA_SA_SA_S6_PDF16_S6_SD_SC_SA_
		.amdhsa_group_segment_fixed_size 32000
		.amdhsa_private_segment_fixed_size 0
		.amdhsa_kernarg_size 392
		.amdhsa_user_sgpr_count 2
		.amdhsa_user_sgpr_dispatch_ptr 0
		.amdhsa_user_sgpr_queue_ptr 0
		.amdhsa_user_sgpr_kernarg_segment_ptr 1
		.amdhsa_user_sgpr_dispatch_id 0
		.amdhsa_user_sgpr_kernarg_preload_length 0
		.amdhsa_user_sgpr_kernarg_preload_offset 0
		.amdhsa_user_sgpr_private_segment_size 0
		.amdhsa_uses_dynamic_stack 0
		.amdhsa_enable_private_segment 0
		.amdhsa_system_sgpr_workgroup_id_x 1
		.amdhsa_system_sgpr_workgroup_id_y 0
		.amdhsa_system_sgpr_workgroup_id_z 0
		.amdhsa_system_sgpr_workgroup_info 0
		.amdhsa_system_vgpr_workitem_id 2
		.amdhsa_next_free_vgpr 128
		.amdhsa_next_free_sgpr 91
		.amdhsa_accum_offset 128
		.amdhsa_reserve_vcc 1
		.amdhsa_float_round_mode_32 0
		.amdhsa_float_round_mode_16_64 0
		.amdhsa_float_denorm_mode_32 3
		.amdhsa_float_denorm_mode_16_64 3
		.amdhsa_dx10_clamp 1
		.amdhsa_ieee_mode 1
		.amdhsa_fp16_overflow 0
		.amdhsa_tg_split 0
		.amdhsa_exception_fp_ieee_invalid_op 0
		.amdhsa_exception_fp_denorm_src 0
		.amdhsa_exception_fp_ieee_div_zero 0
		.amdhsa_exception_fp_ieee_overflow 0
		.amdhsa_exception_fp_ieee_underflow 0
		.amdhsa_exception_fp_ieee_inexact 0
		.amdhsa_exception_int_div_zero 0
	.end_amdhsa_kernel

amdhsa.kernels:
  - .agpr_count:     0
    .args:
      - .actual_access:  read_only
        .address_space:  global
        .offset:         0
        .size:           8
        .value_kind:     global_buffer
      - .actual_access:  read_only
        .address_space:  global
        .offset:         8
        .size:           8
        .value_kind:     global_buffer
      - .actual_access:  read_only
        .address_space:  global
        .offset:         16
        .size:           8
        .value_kind:     global_buffer
      - .actual_access:  read_only
        .address_space:  global
        .offset:         24
        .size:           8
        .value_kind:     global_buffer
      - .actual_access:  write_only
        .address_space:  global
        .offset:         32
        .size:           8
        .value_kind:     global_buffer
      - .actual_access:  write_only
        .address_space:  global
        .offset:         40
        .size:           8
        .value_kind:     global_buffer
    .group_segment_fixed_size: 56512
    .kernarg_segment_align: 8
    .kernarg_segment_size: 48
    .language:       OpenCL C
    .language_version:
      - 2
      - 0
    .max_flat_workgroup_size: 1024
    .name:           _Z10k_bscatterPKiS0_PKfS0_PiP15HIP_vector_typeIiLj2EE
    .private_segment_fixed_size: 0
    .sgpr_count:     42
    .sgpr_spill_count: 0
    .symbol:         _Z10k_bscatterPKiS0_PKfS0_PiP15HIP_vector_typeIiLj2EE.kd
    .uniform_work_group_size: 1
    .uses_dynamic_stack: false
    .vgpr_count:     89
    .vgpr_spill_count: 0
    .wavefront_size: 64
  - .agpr_count:     0
    .args:
      - .actual_access:  read_only
        .address_space:  global
        .offset:         0
        .size:           8
        .value_kind:     global_buffer
      - .actual_access:  read_only
        .address_space:  global
        .offset:         8
        .size:           8
        .value_kind:     global_buffer
      - .actual_access:  write_only
        .address_space:  global
        .offset:         16
        .size:           8
        .value_kind:     global_buffer
      - .actual_access:  write_only
        .address_space:  global
        .offset:         24
        .size:           8
        .value_kind:     global_buffer
      - .actual_access:  write_only
        .address_space:  global
        .offset:         32
        .size:           8
        .value_kind:     global_buffer
      - .actual_access:  write_only
        .address_space:  global
        .offset:         40
        .size:           8
        .value_kind:     global_buffer
      - .actual_access:  read_only
        .address_space:  global
        .offset:         48
        .size:           8
        .value_kind:     global_buffer
      - .actual_access:  write_only
        .address_space:  global
        .offset:         56
        .size:           8
        .value_kind:     global_buffer
    .group_segment_fixed_size: 12352
    .kernarg_segment_align: 8
    .kernarg_segment_size: 64
    .language:       OpenCL C
    .language_version:
      - 2
      - 0
    .max_flat_workgroup_size: 1024
    .name:           _Z8k_bfinalPK15HIP_vector_typeIiLj2EEPKiPS0_PiS6_PfPKfPDF16_
    .private_segment_fixed_size: 0
    .sgpr_count:     38
    .sgpr_spill_count: 0
    .symbol:         _Z8k_bfinalPK15HIP_vector_typeIiLj2EEPKiPS0_PiS6_PfPKfPDF16_.kd
    .uniform_work_group_size: 1
    .uses_dynamic_stack: false
    .vgpr_count:     72
    .vgpr_spill_count: 0
    .wavefront_size: 64
  - .agpr_count:     0
    .args:
      - .actual_access:  read_only
        .address_space:  global
        .offset:         0
        .size:           8
        .value_kind:     global_buffer
      - .actual_access:  write_only
        .address_space:  global
        .offset:         8
        .size:           8
        .value_kind:     global_buffer
      - .actual_access:  write_only
        .address_space:  global
        .offset:         16
        .size:           8
        .value_kind:     global_buffer
      - .actual_access:  read_only
        .address_space:  global
        .offset:         24
        .size:           8
        .value_kind:     global_buffer
      - .actual_access:  read_only
        .address_space:  global
        .offset:         32
        .size:           8
        .value_kind:     global_buffer
      - .actual_access:  write_only
        .address_space:  global
        .offset:         40
        .size:           8
        .value_kind:     global_buffer
      - .actual_access:  read_only
        .address_space:  global
        .offset:         48
        .size:           8
        .value_kind:     global_buffer
      - .actual_access:  read_only
        .address_space:  global
        .offset:         56
        .size:           8
        .value_kind:     global_buffer
      - .actual_access:  read_only
        .address_space:  global
        .offset:         64
        .size:           8
        .value_kind:     global_buffer
      - .actual_access:  read_only
        .address_space:  global
        .offset:         72
        .size:           8
        .value_kind:     global_buffer
      - .actual_access:  read_only
        .address_space:  global
        .offset:         80
        .size:           8
        .value_kind:     global_buffer
      - .actual_access:  read_only
        .address_space:  global
        .offset:         88
        .size:           8
        .value_kind:     global_buffer
      - .actual_access:  write_only
        .address_space:  global
        .offset:         96
        .size:           8
        .value_kind:     global_buffer
      - .actual_access:  write_only
        .address_space:  global
        .offset:         104
        .size:           8
        .value_kind:     global_buffer
      - .actual_access:  write_only
        .address_space:  global
        .offset:         112
        .size:           8
        .value_kind:     global_buffer
      - .actual_access:  write_only
        .address_space:  global
        .offset:         120
        .size:           8
        .value_kind:     global_buffer
      - .actual_access:  write_only
        .address_space:  global
        .offset:         128
        .size:           8
        .value_kind:     global_buffer
    .group_segment_fixed_size: 628
    .kernarg_segment_align: 8
    .kernarg_segment_size: 136
    .language:       OpenCL C
    .language_version:
      - 2
      - 0
    .max_flat_workgroup_size: 1024
    .name:           _Z7k_bhistPKiPiPfPKfS4_PDF16_S4_S4_S4_S4_S4_S4_S5_S5_S5_S5_S2_
    .private_segment_fixed_size: 0
    .sgpr_count:     25
    .sgpr_spill_count: 0
    .symbol:         _Z7k_bhistPKiPiPfPKfS4_PDF16_S4_S4_S4_S4_S4_S4_S5_S5_S5_S5_S2_.kd
    .uniform_work_group_size: 1
    .uses_dynamic_stack: false
    .vgpr_count:     32
    .vgpr_spill_count: 0
    .wavefront_size: 64
  - .agpr_count:     0
    .args:
      - .actual_access:  read_only
        .address_space:  global
        .offset:         0
        .size:           8
        .value_kind:     global_buffer
      - .actual_access:  read_only
        .address_space:  global
        .offset:         8
        .size:           8
        .value_kind:     global_buffer
      - .actual_access:  read_only
        .address_space:  global
        .offset:         16
        .size:           8
        .value_kind:     global_buffer
      - .actual_access:  read_only
        .address_space:  global
        .offset:         24
        .size:           8
        .value_kind:     global_buffer
      - .actual_access:  read_only
        .address_space:  global
        .offset:         32
        .size:           8
        .value_kind:     global_buffer
      - .actual_access:  read_only
        .address_space:  global
        .offset:         40
        .size:           8
        .value_kind:     global_buffer
      - .actual_access:  read_only
        .address_space:  global
        .offset:         48
        .size:           8
        .value_kind:     global_buffer
      - .actual_access:  read_only
        .address_space:  global
        .offset:         56
        .size:           8
        .value_kind:     global_buffer
      - .actual_access:  read_only
        .address_space:  global
        .offset:         64
        .size:           8
        .value_kind:     global_buffer
      - .actual_access:  write_only
        .address_space:  global
        .offset:         72
        .size:           8
        .value_kind:     global_buffer
      - .actual_access:  write_only
        .address_space:  global
        .offset:         80
        .size:           8
        .value_kind:     global_buffer
      - .offset:         88
        .size:           4
        .value_kind:     hidden_block_count_x
      - .offset:         92
        .size:           4
        .value_kind:     hidden_block_count_y
      - .offset:         96
        .size:           4
        .value_kind:     hidden_block_count_z
      - .offset:         100
        .size:           2
        .value_kind:     hidden_group_size_x
      - .offset:         102
        .size:           2
        .value_kind:     hidden_group_size_y
      - .offset:         104
        .size:           2
        .value_kind:     hidden_group_size_z
      - .offset:         106
        .size:           2
        .value_kind:     hidden_remainder_x
      - .offset:         108
        .size:           2
        .value_kind:     hidden_remainder_y
      - .offset:         110
        .size:           2
        .value_kind:     hidden_remainder_z
      - .offset:         128
        .size:           8
        .value_kind:     hidden_global_offset_x
      - .offset:         136
        .size:           8
        .value_kind:     hidden_global_offset_y
      - .offset:         144
        .size:           8
        .value_kind:     hidden_global_offset_z
      - .offset:         152
        .size:           2
        .value_kind:     hidden_grid_dims
    .group_segment_fixed_size: 2048
    .kernarg_segment_align: 8
    .kernarg_segment_size: 344
    .language:       OpenCL C
    .language_version:
      - 2
      - 0
    .max_flat_workgroup_size: 256
    .name:           _Z7k_fold2PKfS0_S0_S0_S0_S0_S0_S0_S0_PDF16_Pf
    .private_segment_fixed_size: 0
    .sgpr_count:     36
    .sgpr_spill_count: 0
    .symbol:         _Z7k_fold2PKfS0_S0_S0_S0_S0_S0_S0_S0_PDF16_Pf.kd
    .uniform_work_group_size: 1
    .uses_dynamic_stack: false
    .vgpr_count:     61
    .vgpr_spill_count: 0
    .wavefront_size: 64
  - .agpr_count:     0
    .args:
      - .actual_access:  read_only
        .address_space:  global
        .offset:         0
        .size:           8
        .value_kind:     global_buffer
      - .actual_access:  read_only
        .address_space:  global
        .offset:         8
        .size:           8
        .value_kind:     global_buffer
      - .actual_access:  write_only
        .address_space:  global
        .offset:         16
        .size:           8
        .value_kind:     global_buffer
      - .actual_access:  read_only
        .address_space:  global
        .offset:         24
        .size:           8
        .value_kind:     global_buffer
      - .actual_access:  read_only
        .address_space:  global
        .offset:         32
        .size:           8
        .value_kind:     global_buffer
      - .actual_access:  read_only
        .address_space:  global
        .offset:         40
        .size:           8
        .value_kind:     global_buffer
      - .actual_access:  read_only
        .address_space:  global
        .offset:         48
        .size:           8
        .value_kind:     global_buffer
      - .actual_access:  read_only
        .address_space:  global
        .offset:         56
        .size:           8
        .value_kind:     global_buffer
      - .actual_access:  read_only
        .address_space:  global
        .offset:         64
        .size:           8
        .value_kind:     global_buffer
      - .actual_access:  read_only
        .address_space:  global
        .offset:         72
        .size:           8
        .value_kind:     global_buffer
      - .actual_access:  read_only
        .address_space:  global
        .offset:         80
        .size:           8
        .value_kind:     global_buffer
      - .actual_access:  write_only
        .address_space:  global
        .offset:         88
        .size:           8
        .value_kind:     global_buffer
      - .actual_access:  write_only
        .address_space:  global
        .offset:         96
        .size:           8
        .value_kind:     global_buffer
      - .address_space:  global
        .offset:         104
        .size:           8
        .value_kind:     global_buffer
      - .actual_access:  write_only
        .address_space:  global
        .offset:         112
        .size:           8
        .value_kind:     global_buffer
      - .actual_access:  read_only
        .address_space:  global
        .offset:         120
        .size:           8
        .value_kind:     global_buffer
      - .actual_access:  read_only
        .address_space:  global
        .offset:         128
        .size:           8
        .value_kind:     global_buffer
    .group_segment_fixed_size: 22272
    .kernarg_segment_align: 8
    .kernarg_segment_size: 136
    .language:       OpenCL C
    .language_version:
      - 2
      - 0
    .max_flat_workgroup_size: 256
    .name:           _Z5k_gcnILi1EEvPKvPK15HIP_vector_typeIiLj2EEPfPKiS8_PKfPKDF16_SA_SA_SA_SA_S6_PDF16_S6_SD_SC_SA_
    .private_segment_fixed_size: 0
    .sgpr_count:     35
    .sgpr_spill_count: 0
    .symbol:         _Z5k_gcnILi1EEvPKvPK15HIP_vector_typeIiLj2EEPfPKiS8_PKfPKDF16_SA_SA_SA_SA_S6_PDF16_S6_SD_SC_SA_.kd
    .uniform_work_group_size: 1
    .uses_dynamic_stack: false
    .vgpr_count:     72
    .vgpr_spill_count: 0
    .wavefront_size: 64
  - .agpr_count:     0
    .args:
      - .actual_access:  read_only
        .address_space:  global
        .offset:         0
        .size:           8
        .value_kind:     global_buffer
      - .actual_access:  read_only
        .address_space:  global
        .offset:         8
        .size:           8
        .value_kind:     global_buffer
      - .actual_access:  read_only
        .address_space:  global
        .offset:         16
        .size:           8
        .value_kind:     global_buffer
      - .actual_access:  read_only
        .address_space:  global
        .offset:         24
        .size:           8
        .value_kind:     global_buffer
      - .actual_access:  read_only
        .address_space:  global
        .offset:         32
        .size:           8
        .value_kind:     global_buffer
      - .actual_access:  read_only
        .address_space:  global
        .offset:         40
        .size:           8
        .value_kind:     global_buffer
      - .actual_access:  read_only
        .address_space:  global
        .offset:         48
        .size:           8
        .value_kind:     global_buffer
      - .actual_access:  read_only
        .address_space:  global
        .offset:         56
        .size:           8
        .value_kind:     global_buffer
      - .actual_access:  read_only
        .address_space:  global
        .offset:         64
        .size:           8
        .value_kind:     global_buffer
      - .actual_access:  read_only
        .address_space:  global
        .offset:         72
        .size:           8
        .value_kind:     global_buffer
      - .actual_access:  read_only
        .address_space:  global
        .offset:         80
        .size:           8
        .value_kind:     global_buffer
      - .actual_access:  read_only
        .address_space:  global
        .offset:         88
        .size:           8
        .value_kind:     global_buffer
      - .actual_access:  write_only
        .address_space:  global
        .offset:         96
        .size:           8
        .value_kind:     global_buffer
      - .address_space:  global
        .offset:         104
        .size:           8
        .value_kind:     global_buffer
      - .actual_access:  read_only
        .address_space:  global
        .offset:         112
        .size:           8
        .value_kind:     global_buffer
      - .actual_access:  read_only
        .address_space:  global
        .offset:         120
        .size:           8
        .value_kind:     global_buffer
      - .actual_access:  read_only
        .address_space:  global
        .offset:         128
        .size:           8
        .value_kind:     global_buffer
      - .offset:         136
        .size:           4
        .value_kind:     hidden_block_count_x
      - .offset:         140
        .size:           4
        .value_kind:     hidden_block_count_y
      - .offset:         144
        .size:           4
        .value_kind:     hidden_block_count_z
      - .offset:         148
        .size:           2
        .value_kind:     hidden_group_size_x
      - .offset:         150
        .size:           2
        .value_kind:     hidden_group_size_y
      - .offset:         152
        .size:           2
        .value_kind:     hidden_group_size_z
      - .offset:         154
        .size:           2
        .value_kind:     hidden_remainder_x
      - .offset:         156
        .size:           2
        .value_kind:     hidden_remainder_y
      - .offset:         158
        .size:           2
        .value_kind:     hidden_remainder_z
      - .offset:         176
        .size:           8
        .value_kind:     hidden_global_offset_x
      - .offset:         184
        .size:           8
        .value_kind:     hidden_global_offset_y
      - .offset:         192
        .size:           8
        .value_kind:     hidden_global_offset_z
      - .offset:         200
        .size:           2
        .value_kind:     hidden_grid_dims
    .group_segment_fixed_size: 32000
    .kernarg_segment_align: 8
    .kernarg_segment_size: 392
    .language:       OpenCL C
    .language_version:
      - 2
      - 0
    .max_flat_workgroup_size: 256
    .name:           _Z5k_gcnILi2EEvPKvPK15HIP_vector_typeIiLj2EEPfPKiS8_PKfPKDF16_SA_SA_SA_SA_S6_PDF16_S6_SD_SC_SA_
    .private_segment_fixed_size: 0
    .sgpr_count:     36
    .sgpr_spill_count: 0
    .symbol:         _Z5k_gcnILi2EEvPKvPK15HIP_vector_typeIiLj2EEPfPKiS8_PKfPKDF16_SA_SA_SA_SA_S6_PDF16_S6_SD_SC_SA_.kd
    .uniform_work_group_size: 1
    .uses_dynamic_stack: false
    .vgpr_count:     128
    .vgpr_spill_count: 0
    .wavefront_size: 64
  - .agpr_count:     0
    .args:
      - .actual_access:  read_only
        .address_space:  global
        .offset:         0
        .size:           8
        .value_kind:     global_buffer
      - .actual_access:  read_only
        .address_space:  global
        .offset:         8
        .size:           8
        .value_kind:     global_buffer
      - .actual_access:  read_only
        .address_space:  global
        .offset:         16
        .size:           8
        .value_kind:     global_buffer
      - .actual_access:  read_only
        .address_space:  global
        .offset:         24
        .size:           8
        .value_kind:     global_buffer
      - .actual_access:  write_only
        .address_space:  global
        .offset:         32
        .size:           8
        .value_kind:     global_buffer
      - .actual_access:  read_only
        .address_space:  global
        .offset:         40
        .size:           8
        .value_kind:     global_buffer
      - .actual_access:  read_only
        .address_space:  global
        .offset:         48
        .size:           8
        .value_kind:     global_buffer
      - .actual_access:  read_only
        .address_space:  global
        .offset:         56
        .size:           8
        .value_kind:     global_buffer
      - .actual_access:  read_only
        .address_space:  global
        .offset:         64
        .size:           8
        .value_kind:     global_buffer
      - .actual_access:  read_only
        .address_space:  global
        .offset:         72
        .size:           8
        .value_kind:     global_buffer
      - .actual_access:  read_only
        .address_space:  global
        .offset:         80
        .size:           8
        .value_kind:     global_buffer
      - .actual_access:  read_only
        .address_space:  global
        .offset:         88
        .size:           8
        .value_kind:     global_buffer
      - .actual_access:  write_only
        .address_space:  global
        .offset:         96
        .size:           8
        .value_kind:     global_buffer
    .group_segment_fixed_size: 9216
    .kernarg_segment_align: 8
    .kernarg_segment_size: 104
    .language:       OpenCL C
    .language_version:
      - 2
      - 0
    .max_flat_workgroup_size: 512
    .name:           _Z6k_lstmILi256ELi10ELb1ELb0EEvPKDF16_S1_S1_PKfPDF16_S1_S1_S1_S3_S3_S3_PfS5_
    .private_segment_fixed_size: 0
    .sgpr_count:     37
    .sgpr_spill_count: 0
    .symbol:         _Z6k_lstmILi256ELi10ELb1ELb0EEvPKDF16_S1_S1_PKfPDF16_S1_S1_S1_S3_S3_S3_PfS5_.kd
    .uniform_work_group_size: 1
    .uses_dynamic_stack: false
    .vgpr_count:     256
    .vgpr_spill_count: 0
    .wavefront_size: 64
  - .agpr_count:     0
    .args:
      - .actual_access:  read_only
        .address_space:  global
        .offset:         0
        .size:           8
        .value_kind:     global_buffer
      - .actual_access:  read_only
        .address_space:  global
        .offset:         8
        .size:           8
        .value_kind:     global_buffer
      - .actual_access:  read_only
        .address_space:  global
        .offset:         16
        .size:           8
        .value_kind:     global_buffer
      - .actual_access:  read_only
        .address_space:  global
        .offset:         24
        .size:           8
        .value_kind:     global_buffer
      - .actual_access:  read_only
        .address_space:  global
        .offset:         32
        .size:           8
        .value_kind:     global_buffer
      - .actual_access:  read_only
        .address_space:  global
        .offset:         40
        .size:           8
        .value_kind:     global_buffer
      - .actual_access:  read_only
        .address_space:  global
        .offset:         48
        .size:           8
        .value_kind:     global_buffer
      - .actual_access:  read_only
        .address_space:  global
        .offset:         56
        .size:           8
        .value_kind:     global_buffer
      - .actual_access:  read_only
        .address_space:  global
        .offset:         64
        .size:           8
        .value_kind:     global_buffer
      - .actual_access:  read_only
        .address_space:  global
        .offset:         72
        .size:           8
        .value_kind:     global_buffer
      - .actual_access:  read_only
        .address_space:  global
        .offset:         80
        .size:           8
        .value_kind:     global_buffer
      - .actual_access:  write_only
        .address_space:  global
        .offset:         88
        .size:           8
        .value_kind:     global_buffer
      - .actual_access:  read_only
        .address_space:  global
        .offset:         96
        .size:           8
        .value_kind:     global_buffer
    .group_segment_fixed_size: 0
    .kernarg_segment_align: 8
    .kernarg_segment_size: 104
    .language:       OpenCL C
    .language_version:
      - 2
      - 0
    .max_flat_workgroup_size: 512
    .name:           _Z6k_lstmILi128ELi8ELb0ELb1EEvPKDF16_S1_S1_PKfPDF16_S1_S1_S1_S3_S3_S3_PfS5_
    .private_segment_fixed_size: 0
    .sgpr_count:     46
    .sgpr_spill_count: 0
    .symbol:         _Z6k_lstmILi128ELi8ELb0ELb1EEvPKDF16_S1_S1_PKfPDF16_S1_S1_S1_S3_S3_S3_PfS5_.kd
    .uniform_work_group_size: 1
    .uses_dynamic_stack: false
    .vgpr_count:     256
    .vgpr_spill_count: 0
    .wavefront_size: 64
